# speedup vs baseline: 1.0685x; 1.0249x over previous
_Z8gemm_f16ILi256ELi160ELi4ELi2ELi2ELi1ELi1EEvPKDF16_S1_Pviiii:
	s_load_dwordx4 s[12:15], s[0:1], 0x0
	s_load_dwordx2 s[0:1], s[0:1], 0x10
	s_lshl_b32 s3, s2, 8
	s_and_b32 s10, s3, 0x700
	s_lshr_b32 s2, s2, 3
	s_mulk_i32 s2, 0xa0
	s_movk_i32 s5, 0x12c0
	v_lshrrev_b32_e32 v95, 3, v0
	v_and_b32_e32 v99, 7, v0
	v_bfe_u32 v91, v0, 4, 3
	v_xor_b32_e32 v99, v99, v91
	v_lshlrev_b32_e32 v99, 4, v99
	v_add_u32_e32 v91, s10, v95
	v_lshl_add_u32 v82, v91, 11, v99
	v_add_u32_e32 v83, 0x20000, v82
	v_add_u32_e32 v84, 0x40000, v82
	v_add_u32_e32 v85, 0x60000, v82
	v_add_u32_e32 v91, s2, v95
	v_lshl_add_u32 v86, v91, 11, v99
	v_add_u32_e32 v87, 0x20000, v86
	v_add_u32_e32 v88, 0x40000, v86
	v_lshlrev_b32_e32 v95, 4, v0
	s_nop 0
	v_readfirstlane_b32 s20, v95
	s_mov_b32 s29, 0xa000
	s_cmp_lt_u32 s20, 0x1000
	s_cselect_b32 s29, 0xc000, s29
	s_cbranch_scc1 .Lg1_w03
	v_mov_b32_e32 v88, v87
.Lg1_w03:
	v_and_b32_e32 v98, 15, v0
	v_bfe_u32 v97, v0, 4, 2
	v_lshrrev_b32_e32 v96, 7, v0
	v_bfe_u32 v1, v0, 6, 1
	v_bfe_u32 v95, v0, 1, 3
	v_xor_b32_e32 v95, v97, v95
	v_lshlrev_b32_e32 v95, 4, v95
	v_lshl_or_b32 v99, v98, 7, v95
	v_lshl_or_b32 v89, v96, 13, v99
	v_mul_u32_u24_e32 v95, 0x2800, v1
	v_add_u32_e32 v95, 0x8000, v95
	v_add_u32_e32 v90, v95, v99
	s_waitcnt lgkmcnt(0)
	s_mov_b32 s22, s12
	s_mov_b32 s23, s13
	s_mov_b32 s24, s14
	s_mov_b32 s25, s15
	s_mov_b32 s26, s20
	s_add_i32 s30, s26, s29
	s_mov_b32 m0, s26
	s_add_i32 s26, s26, 0x2000
	global_load_lds_dwordx4 v82, s[22:23]
	s_mov_b32 m0, s26
	s_add_i32 s26, s26, 0x2000
	global_load_lds_dwordx4 v83, s[22:23]
	s_mov_b32 m0, s26
	s_add_i32 s26, s26, 0x2000
	global_load_lds_dwordx4 v84, s[22:23]
	s_mov_b32 m0, s26
	s_add_i32 s26, s26, 0x2000
	global_load_lds_dwordx4 v85, s[22:23]
	s_mov_b32 m0, s26
	s_add_i32 s26, s26, 0x2000
	global_load_lds_dwordx4 v86, s[24:25]
	s_mov_b32 m0, s26
	s_add_i32 s26, s26, 0x2000
	global_load_lds_dwordx4 v87, s[24:25]
	s_mov_b32 m0, s30
	s_add_i32 s26, s26, 0x1000
	global_load_lds_dwordx4 v88, s[24:25]
	s_add_u32 s22, s22, 0x80
	s_addc_u32 s23, s23, 0
	s_add_u32 s24, s24, 0x80
	s_addc_u32 s25, s25, 0
	s_add_i32 s30, s26, s29
	s_mov_b32 m0, s26
	s_add_i32 s26, s26, 0x2000
	global_load_lds_dwordx4 v82, s[22:23]
	s_mov_b32 m0, s26
	s_add_i32 s26, s26, 0x2000
	global_load_lds_dwordx4 v83, s[22:23]
	s_mov_b32 m0, s26
	s_add_i32 s26, s26, 0x2000
	global_load_lds_dwordx4 v84, s[22:23]
	s_mov_b32 m0, s26
	s_add_i32 s26, s26, 0x2000
	global_load_lds_dwordx4 v85, s[22:23]
	s_mov_b32 m0, s26
	s_add_i32 s26, s26, 0x2000
	global_load_lds_dwordx4 v86, s[24:25]
	s_mov_b32 m0, s26
	s_add_i32 s26, s26, 0x2000
	global_load_lds_dwordx4 v87, s[24:25]
	s_mov_b32 m0, s30
	s_add_i32 s26, s26, 0x1000
	global_load_lds_dwordx4 v88, s[24:25]
	s_add_u32 s22, s22, 0x80
	s_addc_u32 s23, s23, 0
	s_add_u32 s24, s24, 0x80
	s_addc_u32 s25, s25, 0
	s_add_i32 s30, s26, s29
	s_mov_b32 m0, s26
	s_add_i32 s26, s26, 0x2000
	global_load_lds_dwordx4 v82, s[22:23]
	s_mov_b32 m0, s26
	s_add_i32 s26, s26, 0x2000
	global_load_lds_dwordx4 v83, s[22:23]
	s_mov_b32 m0, s26
	s_add_i32 s26, s26, 0x2000
	global_load_lds_dwordx4 v84, s[22:23]
	s_mov_b32 m0, s26
	s_add_i32 s26, s26, 0x2000
	global_load_lds_dwordx4 v85, s[22:23]
	s_mov_b32 m0, s26
	s_add_i32 s26, s26, 0x2000
	global_load_lds_dwordx4 v86, s[24:25]
	s_mov_b32 m0, s26
	s_add_i32 s26, s26, 0x2000
	global_load_lds_dwordx4 v87, s[24:25]
	s_mov_b32 m0, s30
	s_add_i32 s26, s26, 0x1000
	global_load_lds_dwordx4 v88, s[24:25]
	v_mov_b32_e32 v2, 0
	v_mov_b32_e32 v3, 0
	v_mov_b32_e32 v4, 0
	v_mov_b32_e32 v5, 0
	v_mov_b32_e32 v6, 0
	v_mov_b32_e32 v7, 0
	v_mov_b32_e32 v8, 0
	v_mov_b32_e32 v9, 0
	v_mov_b32_e32 v10, 0
	v_mov_b32_e32 v11, 0
	v_mov_b32_e32 v12, 0
	v_mov_b32_e32 v13, 0
	v_mov_b32_e32 v14, 0
	v_mov_b32_e32 v15, 0
	v_mov_b32_e32 v16, 0
	v_mov_b32_e32 v17, 0
	v_mov_b32_e32 v18, 0
	v_mov_b32_e32 v19, 0
	v_mov_b32_e32 v20, 0
	v_mov_b32_e32 v21, 0
	v_mov_b32_e32 v22, 0
	v_mov_b32_e32 v23, 0
	v_mov_b32_e32 v24, 0
	v_mov_b32_e32 v25, 0
	v_mov_b32_e32 v26, 0
	v_mov_b32_e32 v27, 0
	v_mov_b32_e32 v28, 0
	v_mov_b32_e32 v29, 0
	v_mov_b32_e32 v30, 0
	v_mov_b32_e32 v31, 0
	v_mov_b32_e32 v32, 0
	v_mov_b32_e32 v33, 0
	v_mov_b32_e32 v34, 0
	v_mov_b32_e32 v35, 0
	v_mov_b32_e32 v36, 0
	v_mov_b32_e32 v37, 0
	v_mov_b32_e32 v38, 0
	v_mov_b32_e32 v39, 0
	v_mov_b32_e32 v40, 0
	v_mov_b32_e32 v41, 0
	v_mov_b32_e32 v42, 0
	v_mov_b32_e32 v43, 0
	v_mov_b32_e32 v44, 0
	v_mov_b32_e32 v45, 0
	v_mov_b32_e32 v46, 0
	v_mov_b32_e32 v47, 0
	v_mov_b32_e32 v48, 0
	v_mov_b32_e32 v49, 0
	v_mov_b32_e32 v50, 0
	v_mov_b32_e32 v51, 0
	v_mov_b32_e32 v52, 0
	v_mov_b32_e32 v53, 0
	v_mov_b32_e32 v54, 0
	v_mov_b32_e32 v55, 0
	v_mov_b32_e32 v56, 0
	v_mov_b32_e32 v57, 0
	v_mov_b32_e32 v58, 0
	v_mov_b32_e32 v59, 0
	v_mov_b32_e32 v60, 0
	v_mov_b32_e32 v61, 0
	v_mov_b32_e32 v62, 0
	v_mov_b32_e32 v63, 0
	v_mov_b32_e32 v64, 0
	v_mov_b32_e32 v65, 0
	v_mov_b32_e32 v66, 0
	v_mov_b32_e32 v67, 0
	v_mov_b32_e32 v68, 0
	v_mov_b32_e32 v69, 0
	v_mov_b32_e32 v70, 0
	v_mov_b32_e32 v71, 0
	v_mov_b32_e32 v72, 0
	v_mov_b32_e32 v73, 0
	v_mov_b32_e32 v74, 0
	v_mov_b32_e32 v75, 0
	v_mov_b32_e32 v76, 0
	v_mov_b32_e32 v77, 0
	v_mov_b32_e32 v78, 0
	v_mov_b32_e32 v79, 0
	v_mov_b32_e32 v80, 0
	v_mov_b32_e32 v81, 0
	s_mov_b32 s16, 0
	s_mov_b32 s17, 0
	v_mov_b32_e32 v91, v89
	v_mov_b32_e32 v93, v90
	v_xor_b32_e32 v92, 64, v89
	v_xor_b32_e32 v94, 64, v90
	s_waitcnt vmcnt(14)
	s_barrier
	ds_read_b128 v[116:119], v93
	ds_read_b128 v[100:103], v91
	ds_read_b128 v[120:123], v93 offset:2048
	ds_read_b128 v[104:107], v91 offset:2048
	ds_read_b128 v[124:127], v93 offset:4096
	ds_read_b128 v[108:111], v91 offset:4096
	ds_read_b128 v[128:131], v93 offset:6144
	ds_read_b128 v[112:115], v91 offset:6144
	ds_read_b128 v[132:135], v93 offset:8192
.Lg1_loop:
	ds_read_b128 v[152:155], v94
	ds_read_b128 v[136:139], v92
	ds_read_b128 v[156:159], v94 offset:2048
	ds_read_b128 v[140:143], v92 offset:2048
	ds_read_b128 v[160:163], v94 offset:4096
	ds_read_b128 v[144:147], v92 offset:4096
	s_add_i32 s18, s16, 3
	s_min_i32 s18, s18, 15
	s_lshl_b32 s18, s18, 7
	s_add_u32 s22, s12, s18
	s_addc_u32 s23, s13, 0
	s_add_u32 s24, s14, s18
	s_addc_u32 s25, s15, 0
	s_add_i32 s26, s17, s20
	s_add_i32 s30, s26, s29
	s_add_i32 s27, s17, 0xd000
	s_cmp_lg_u32 s27, 0x27000
	s_cselect_b32 s27, s27, 0
	s_waitcnt lgkmcnt(6)
	v_mfma_f32_16x16x32_f16 v[34:37], v[116:119], v[100:103], v[34:37]
	v_mfma_f32_16x16x32_f16 v[78:81], v[120:123], v[100:103], v[78:81]
	ds_read_b128 v[164:167], v94 offset:6144
	v_mfma_f32_16x16x32_f16 v[74:77], v[124:127], v[100:103], v[74:77]
	ds_read_b128 v[148:151], v92 offset:6144
	v_mfma_f32_16x16x32_f16 v[70:73], v[128:131], v[100:103], v[70:73]
	ds_read_b128 v[168:171], v94 offset:8192
	v_mfma_f32_16x16x32_f16 v[62:65], v[132:135], v[100:103], v[62:65]
	v_mfma_f32_16x16x32_f16 v[58:61], v[116:119], v[104:107], v[58:61]
	v_mfma_f32_16x16x32_f16 v[54:57], v[120:123], v[104:107], v[54:57]
	v_add_u32_e32 v91, s27, v89
	v_mfma_f32_16x16x32_f16 v[50:53], v[124:127], v[104:107], v[50:53]
	v_mfma_f32_16x16x32_f16 v[46:49], v[128:131], v[104:107], v[46:49]
	v_add_u32_e32 v93, s27, v90
	v_mfma_f32_16x16x32_f16 v[42:45], v[132:135], v[104:107], v[42:45]
	v_mfma_f32_16x16x32_f16 v[38:41], v[116:119], v[108:111], v[38:41]
	v_xor_b32_e32 v92, 64, v91
	v_mfma_f32_16x16x32_f16 v[30:33], v[120:123], v[108:111], v[30:33]
	v_mfma_f32_16x16x32_f16 v[26:29], v[124:127], v[108:111], v[26:29]
	v_xor_b32_e32 v94, 64, v93
	v_mfma_f32_16x16x32_f16 v[22:25], v[128:131], v[108:111], v[22:25]
	v_mfma_f32_16x16x32_f16 v[18:21], v[132:135], v[108:111], v[18:21]
	v_mfma_f32_16x16x32_f16 v[14:17], v[116:119], v[112:115], v[14:17]
	v_mfma_f32_16x16x32_f16 v[10:13], v[120:123], v[112:115], v[10:13]
	v_mfma_f32_16x16x32_f16 v[2:5], v[124:127], v[112:115], v[2:5]
	v_mfma_f32_16x16x32_f16 v[6:9], v[128:131], v[112:115], v[6:9]
	v_mfma_f32_16x16x32_f16 v[66:69], v[132:135], v[112:115], v[66:69]
	s_waitcnt vmcnt(7)
	s_waitcnt lgkmcnt(0)
	s_barrier
	ds_read_b128 v[116:119], v93
	ds_read_b128 v[100:103], v91
	ds_read_b128 v[120:123], v93 offset:2048
	ds_read_b128 v[104:107], v91 offset:2048
	ds_read_b128 v[124:127], v93 offset:4096
	ds_read_b128 v[108:111], v91 offset:4096
	ds_read_b128 v[128:131], v93 offset:6144
	ds_read_b128 v[112:115], v91 offset:6144
	ds_read_b128 v[132:135], v93 offset:8192
	v_mfma_f32_16x16x32_f16 v[34:37], v[152:155], v[136:139], v[34:37]
	v_mfma_f32_16x16x32_f16 v[78:81], v[156:159], v[136:139], v[78:81]
	v_mfma_f32_16x16x32_f16 v[74:77], v[160:163], v[136:139], v[74:77]
	s_mov_b32 m0, s26
	s_add_i32 s26, s26, 0x2000
	global_load_lds_dwordx4 v82, s[22:23]
	v_mfma_f32_16x16x32_f16 v[70:73], v[164:167], v[136:139], v[70:73]
	v_mfma_f32_16x16x32_f16 v[62:65], v[168:171], v[136:139], v[62:65]
	v_mfma_f32_16x16x32_f16 v[58:61], v[152:155], v[140:143], v[58:61]
	s_mov_b32 m0, s26
	s_add_i32 s26, s26, 0x2000
	global_load_lds_dwordx4 v83, s[22:23]
	v_mfma_f32_16x16x32_f16 v[54:57], v[156:159], v[140:143], v[54:57]
	v_mfma_f32_16x16x32_f16 v[50:53], v[160:163], v[140:143], v[50:53]
	v_mfma_f32_16x16x32_f16 v[46:49], v[164:167], v[140:143], v[46:49]
	s_mov_b32 m0, s26
	s_add_i32 s26, s26, 0x2000
	global_load_lds_dwordx4 v84, s[22:23]
	v_mfma_f32_16x16x32_f16 v[42:45], v[168:171], v[140:143], v[42:45]
	v_mfma_f32_16x16x32_f16 v[38:41], v[152:155], v[144:147], v[38:41]
	v_mfma_f32_16x16x32_f16 v[30:33], v[156:159], v[144:147], v[30:33]
	s_mov_b32 m0, s26
	s_add_i32 s26, s26, 0x2000
	global_load_lds_dwordx4 v85, s[22:23]
	v_mfma_f32_16x16x32_f16 v[26:29], v[160:163], v[144:147], v[26:29]
	v_mfma_f32_16x16x32_f16 v[22:25], v[164:167], v[144:147], v[22:25]
	v_mfma_f32_16x16x32_f16 v[18:21], v[168:171], v[144:147], v[18:21]
	s_mov_b32 m0, s26
	s_add_i32 s26, s26, 0x2000
	global_load_lds_dwordx4 v86, s[24:25]
	v_mfma_f32_16x16x32_f16 v[14:17], v[152:155], v[148:151], v[14:17]
	v_mfma_f32_16x16x32_f16 v[10:13], v[156:159], v[148:151], v[10:13]
	v_mfma_f32_16x16x32_f16 v[2:5], v[160:163], v[148:151], v[2:5]
	s_mov_b32 m0, s26
	s_add_i32 s26, s26, 0x2000
	global_load_lds_dwordx4 v87, s[24:25]
	v_mfma_f32_16x16x32_f16 v[6:9], v[164:167], v[148:151], v[6:9]
	v_mfma_f32_16x16x32_f16 v[66:69], v[168:171], v[148:151], v[66:69]
	s_mov_b32 m0, s30
	s_nop 0
	global_load_lds_dwordx4 v88, s[24:25]
	s_mov_b32 s17, s27
	s_add_i32 s16, s16, 1
	s_cmp_lt_u32 s16, 16
	s_cbranch_scc1 .Lg1_loop
	s_nop 7

	.amdhsa_kernel _Z8gemm_f16ILi256ELi160ELi4ELi2ELi2ELi1ELi1EEvPKDF16_S1_Pviiii
		.amdhsa_group_segment_fixed_size 159744
		.amdhsa_private_segment_fixed_size 0
		.amdhsa_kernarg_size 40
		.amdhsa_user_sgpr_count 2
		.amdhsa_user_sgpr_dispatch_ptr 0
		.amdhsa_user_sgpr_queue_ptr 0
		.amdhsa_user_sgpr_kernarg_segment_ptr 1
		.amdhsa_user_sgpr_dispatch_id 0
		.amdhsa_user_sgpr_kernarg_preload_length 0
		.amdhsa_user_sgpr_kernarg_preload_offset 0
		.amdhsa_user_sgpr_private_segment_size 0
		.amdhsa_uses_dynamic_stack 0
		.amdhsa_enable_private_segment 0
		.amdhsa_system_sgpr_workgroup_id_x 1
		.amdhsa_system_sgpr_workgroup_id_y 0
		.amdhsa_system_sgpr_workgroup_id_z 0
		.amdhsa_system_sgpr_workgroup_info 0
		.amdhsa_system_vgpr_workitem_id 0
		.amdhsa_next_free_vgpr 172
		.amdhsa_next_free_sgpr 96
		.amdhsa_accum_offset 172
		.amdhsa_reserve_vcc 1
		.amdhsa_float_round_mode_32 0
		.amdhsa_float_round_mode_16_64 0
		.amdhsa_float_denorm_mode_32 3
		.amdhsa_float_denorm_mode_16_64 3
		.amdhsa_dx10_clamp 1
		.amdhsa_ieee_mode 1
		.amdhsa_fp16_overflow 0
		.amdhsa_tg_split 0
		.amdhsa_exception_fp_ieee_invalid_op 0
		.amdhsa_exception_fp_denorm_src 0
		.amdhsa_exception_fp_ieee_div_zero 0
		.amdhsa_exception_fp_ieee_overflow 0
		.amdhsa_exception_fp_ieee_underflow 0
		.amdhsa_exception_fp_ieee_inexact 0
		.amdhsa_exception_int_div_zero 0
	.end_amdhsa_kernel

amdhsa.kernels:
  - .agpr_count:     0
    .args:
      - .offset:         0
        .size:           88
        .value_kind:     by_value
    .group_segment_fixed_size: 16640
    .kernarg_segment_align: 8
    .kernarg_segment_size: 88
    .language:       OpenCL C
    .language_version:
      - 2
      - 0
    .max_flat_workgroup_size: 256
    .name:           _Z15prologue_kernel7ProArgs
    .private_segment_fixed_size: 0
    .sgpr_count:     28
    .sgpr_spill_count: 0
    .symbol:         _Z15prologue_kernel7ProArgs.kd
    .uniform_work_group_size: 1
    .uses_dynamic_stack: false
    .vgpr_count:     54
    .vgpr_spill_count: 0
    .wavefront_size: 64
  - .agpr_count:     0
    .args:
      - .offset:         0
        .size:           96
        .value_kind:     by_value
    .group_segment_fixed_size: 149760
    .kernarg_segment_align: 8
    .kernarg_segment_size: 96
    .language:       OpenCL C
    .language_version:
      - 2
      - 0
    .max_flat_workgroup_size: 384
    .name:           _Z11prep_kernel8PrepArgs
    .private_segment_fixed_size: 0
    .sgpr_count:     41
    .sgpr_spill_count: 0
    .symbol:         _Z11prep_kernel8PrepArgs.kd
    .uniform_work_group_size: 1
    .uses_dynamic_stack: false
    .vgpr_count:     256
    .vgpr_spill_count: 0
    .wavefront_size: 64
  - .agpr_count:     0
    .args:
      - .actual_access:  read_only
        .address_space:  global
        .offset:         0
        .size:           8
        .value_kind:     global_buffer
      - .actual_access:  read_only
        .address_space:  global
        .offset:         8
        .size:           8
        .value_kind:     global_buffer
      - .actual_access:  read_only
        .address_space:  global
        .offset:         16
        .size:           8
        .value_kind:     global_buffer
      - .actual_access:  read_only
        .address_space:  global
        .offset:         24
        .size:           8
        .value_kind:     global_buffer
      - .actual_access:  write_only
        .address_space:  global
        .offset:         32
        .size:           8
        .value_kind:     global_buffer
      - .actual_access:  write_only
        .address_space:  global
        .offset:         40
        .size:           8
        .value_kind:     global_buffer
    .group_segment_fixed_size: 0
    .kernarg_segment_align: 8
    .kernarg_segment_size: 48
    .language:       OpenCL C
    .language_version:
      - 2
      - 0
    .max_flat_workgroup_size: 64
    .name:           _Z16rec_chunk_kernelPKDF16_PKfS2_S2_PfS3_
    .private_segment_fixed_size: 0
    .sgpr_count:     42
    .sgpr_spill_count: 0
    .symbol:         _Z16rec_chunk_kernelPKDF16_PKfS2_S2_PfS3_.kd
    .uniform_work_group_size: 1
    .uses_dynamic_stack: false
    .vgpr_count:     256
    .vgpr_spill_count: 0
    .wavefront_size: 64
  - .agpr_count:     0
    .args:
      - .actual_access:  read_only
        .address_space:  global
        .offset:         0
        .size:           8
        .value_kind:     global_buffer
      - .actual_access:  read_only
        .address_space:  global
        .offset:         8
        .size:           8
        .value_kind:     global_buffer
      - .actual_access:  read_only
        .address_space:  global
        .offset:         16
        .size:           8
        .value_kind:     global_buffer
      - .actual_access:  write_only
        .address_space:  global
        .offset:         24
        .size:           8
        .value_kind:     global_buffer
      - .actual_access:  read_only
        .address_space:  global
        .offset:         32
        .size:           8
        .value_kind:     global_buffer
      - .actual_access:  write_only
        .address_space:  global
        .offset:         40
        .size:           8
        .value_kind:     global_buffer
    .group_segment_fixed_size: 16640
    .kernarg_segment_align: 8
    .kernarg_segment_size: 48
    .language:       OpenCL C
    .language_version:
      - 2
      - 0
    .max_flat_workgroup_size: 256
    .name:           _Z16norm_gate_kernelPKfPKDF16_S0_PDF16_S0_S3_
    .private_segment_fixed_size: 0
    .sgpr_count:     20
    .sgpr_spill_count: 0
    .symbol:         _Z16norm_gate_kernelPKfPKDF16_S0_PDF16_S0_S3_.kd
    .uniform_work_group_size: 1
    .uses_dynamic_stack: false
    .vgpr_count:     63
    .vgpr_spill_count: 0
    .wavefront_size: 64
  - .agpr_count:     0
    .args:
      - .address_space:  global
        .offset:         0
        .size:           8
        .value_kind:     global_buffer
      - .address_space:  global
        .offset:         8
        .size:           8
        .value_kind:     global_buffer
      - .actual_access:  write_only
        .address_space:  global
        .offset:         16
        .size:           8
        .value_kind:     global_buffer
      - .offset:         24
        .size:           4
        .value_kind:     by_value
      - .offset:         28
        .size:           4
        .value_kind:     by_value
      - .offset:         32
        .size:           4
        .value_kind:     by_value
      - .offset:         36
        .size:           4
        .value_kind:     by_value
    .group_segment_fixed_size: 159744
    .kernarg_segment_align: 8
    .kernarg_segment_size: 40
    .language:       OpenCL C
    .language_version:
      - 2
      - 0
    .max_flat_workgroup_size: 512
    .name:           _Z8gemm_f16ILi256ELi160ELi4ELi2ELi2ELi1ELi1EEvPKDF16_S1_Pviiii
    .private_segment_fixed_size: 0
    .sgpr_count:     22
    .sgpr_spill_count: 0
    .symbol:         _Z8gemm_f16ILi256ELi160ELi4ELi2ELi2ELi1ELi1EEvPKDF16_S1_Pviiii.kd
    .uniform_work_group_size: 1
    .uses_dynamic_stack: false
    .vgpr_count:     172
    .vgpr_spill_count: 0
    .wavefront_size: 64
  - .agpr_count:     32
    .args:
      - .address_space:  global
        .offset:         0
        .size:           8
        .value_kind:     global_buffer
      - .address_space:  global
        .offset:         8
        .size:           8
        .value_kind:     global_buffer
      - .actual_access:  write_only
        .address_space:  global
        .offset:         16
        .size:           8
        .value_kind:     global_buffer
      - .offset:         24
        .size:           4
        .value_kind:     by_value
      - .offset:         28
        .size:           4
        .value_kind:     by_value
      - .offset:         32
        .size:           4
        .value_kind:     by_value
      - .offset:         36
        .size:           4
        .value_kind:     by_value
    .group_segment_fixed_size: 98304
    .kernarg_segment_align: 8
    .kernarg_segment_size: 40
    .language:       OpenCL C
    .language_version:
      - 2
      - 0
    .max_flat_workgroup_size: 256
    .name:           _Z8gemm_f16ILi128ELi64ELi2ELi2ELi4ELi2ELi0EEvPKDF16_S1_Pviiii
    .private_segment_fixed_size: 0
    .sgpr_count:     25
    .sgpr_spill_count: 0
    .symbol:         _Z8gemm_f16ILi128ELi64ELi2ELi2ELi4ELi2ELi0EEvPKDF16_S1_Pviiii.kd
    .uniform_work_group_size: 1
    .uses_dynamic_stack: false
    .vgpr_count:     96
    .vgpr_spill_count: 0
    .wavefront_size: 64
